# inproj: last round split into 128-row half tiles over all 256 workgroups (second A half neither staged nor multiplied), mode-dependent counted waits
# speedup vs baseline: 1.0062x; 1.0035x over previous
.LBB0_131:
	s_add_u32 s4, s0, 0xc100000
	s_addc_u32 s5, s1, 0
	s_lshl_b32 s9, s9, 5
	s_and_b32 s9, s9, 0x60
	s_add_i32 m0, s15, 0x18000
	v_lshl_add_u64 v[8:9], v[8:9], 0, s[46:47]
	s_lshl_b32 s12, s8, 13
	s_lshl_b32 s13, s9, 7
	s_waitcnt vmcnt(2)
	s_barrier
	global_load_lds_dwordx4 v[8:9], off
	v_lshl_add_u64 v[6:7], v[6:7], 0, s[46:47]
	s_add_i32 m0, s15, 0x1a000
	s_add_i32 s38, s15, 0x8000
	s_add_i32 s39, s15, 0xa000
	global_load_lds_dwordx4 v[6:7], off
	v_lshl_add_u64 v[2:3], v[2:3], 0, s[46:47]
	s_mov_b32 m0, s38
	s_add_u32 s10, s18, 0x40080
	global_load_lds_dwordx4 v[2:3], off
	v_lshl_add_u64 v[2:3], v[4:5], 0, s[46:47]
	s_mov_b32 m0, s39
	s_addc_u32 s11, s19, 0
	global_load_lds_dwordx4 v[2:3], off
	s_add_i32 m0, s15, 0x1c000
	v_lshl_add_u64 v[2:3], s[10:11], 0, v[0:1]
	global_load_lds_dwordx4 v[2:3], off
	v_lshl_add_u64 v[2:3], s[10:11], 0, v[134:135]
	s_add_i32 m0, s15, 0x1e000
	s_cmpk_lt_u32 s7, 0x100
	global_load_lds_dwordx4 v[2:3], off
	v_lshrrev_b32_e32 v3, 1, v10
	v_and_b32_e32 v4, 24, v3
	v_and_b32_e32 v2, 15, v10
	v_lshlrev_b32_e32 v3, 1, v4
	s_sext_i32_i8 s50, s6
	v_lshl_or_b32 v162, s8, 6, v2
	v_lshl_or_b32 v2, v2, 6, v3
	v_lshlrev_b32_e32 v3, 2, v10
	s_cselect_b64 s[6:7], -1, 0
	s_ashr_i32 s42, s26, 31
	s_lshl_b32 s8, s9, 2
	v_and_b32_e32 v3, 32, v3
	s_add_u32 s0, s0, s8
	v_bitop3_b32 v5, v2, s12, v3 bitop3:0xde
	v_bitop3_b32 v163, s13, v2, v3 bitop3:0xf6
	s_addc_u32 s1, s1, 0
	v_lshlrev_b32_e32 v2, 2, v4
	v_mov_b32_e32 v3, v1
	v_lshl_add_u64 v[2:3], s[0:1], 0, v[2:3]
	s_mov_b64 s[0:1], 0x13100000
	v_lshl_add_u64 v[140:141], v[2:3], 0, s[0:1]
	v_lshlrev_b32_e32 v2, 14, v11
	v_and_b32_e32 v2, 0xffff8000, v2
	v_lshl_add_u32 v2, v12, 11, v2
	v_and_b32_e32 v3, 1, v11
	v_lshl_or_b32 v2, v3, 6, v2
	v_lshl_add_u32 v142, v13, 1, v2
	v_lshlrev_b32_e32 v2, 14, v15
	v_and_b32_e32 v2, 0xffff8000, v2
	s_waitcnt vmcnt(6)
	v_lshl_add_u32 v2, v14, 11, v2
	v_and_b32_e32 v3, 1, v15
	v_lshl_or_b32 v2, v3, 6, v2
	v_or_b32_e32 v164, s9, v4
	v_mov_b32_e32 v143, v1
	v_lshl_add_u32 v144, v16, 1, v2
	v_mov_b32_e32 v145, v1
	s_mov_b32 s43, 0
	v_add_u32_e32 v165, 0, v5
	s_barrier
	s_mov_b32 s56, 0
	s_branch .LBB0_134

.LBB0_133:
	s_andn2_b64 vcc, exec, s[0:1]
	s_mov_b32 s56, s57
	s_mov_b32 s50, s8
	s_mov_b32 s14, s10
	s_mov_b64 s[18:19], s[16:17]
	s_mov_b64 s[20:21], s[12:13]
	s_cbranch_vccz .LBB0_145
.LBB0_134:
	s_add_i32 s43, s43, 1
	s_mul_i32 s0, s43, s42
	s_mul_hi_u32 s1, s43, s26
	s_add_i32 s1, s1, s0
	s_mul_i32 s0, s43, s26
	s_add_u32 s12, s0, s25
	s_addc_u32 s13, s1, s34
	s_mov_b32 s57, 0
	s_cmpk_lt_u32 s12, 0x300
	s_cbranch_scc1 .Lhf_n
	s_mov_b32 s57, 1
	s_cmpk_lt_u32 s12, 0x380
	s_cbranch_scc1 .Lhf_n
	s_mov_b32 s57, 2
	s_addk_i32 s12, 0xff80
.Lhf_n:
	v_mov_b64_e32 v[2:3], 0x380
	v_cmp_lt_i64_e64 s[0:1], s[12:13], v[2:3]
	v_mov_b64_e32 v[2:3], 0x37f
	v_cmp_gt_i64_e32 vcc, s[12:13], v[2:3]
	s_cbranch_vccnz .LBB0_136
	s_ashr_i32 s8, s12, 31
	s_lshr_b32 s8, s8, 29
	s_add_i32 s8, s12, s8
	s_ashr_i32 s9, s8, 3
	s_and_b32 s8, s8, -8
	s_sub_i32 s8, s12, s8
	s_cmp_lt_i32 s8, 0
	s_movk_i32 s10, 0x71
	s_cselect_b32 s10, s10, 0x70
	s_mul_i32 s8, s10, s8
	s_add_i32 s8, s8, s9
	s_mul_hi_i32 s9, s8, 0x92492493
	s_add_i32 s9, s9, s8
	s_lshr_b32 s10, s9, 31
	s_ashr_i32 s9, s9, 6
	s_add_i32 s9, s9, s10
	s_lshl_b32 s10, s9, 3
	s_sub_i32 s11, 64, s10
	s_min_i32 s11, s11, 8
	s_abs_i32 s12, s11
	v_cvt_f32_u32_e32 v2, s12
	s_sub_i32 s16, 0, s12
	s_mulk_i32 s9, 0x70
	s_sub_i32 s9, s8, s9
	v_rcp_iflag_f32_e32 v2, v2
	s_abs_i32 s8, s9
	s_xor_b32 s13, s9, s11
	s_ashr_i32 s13, s13, 31
	v_mul_f32_e32 v2, 0x4f7ffffe, v2
	v_cvt_u32_f32_e32 v2, v2
	s_nop 0
	v_readfirstlane_b32 s17, v2
	s_mul_i32 s16, s16, s17
	s_mul_hi_u32 s16, s17, s16
	s_add_i32 s17, s17, s16
	s_mul_hi_u32 s16, s8, s17
	s_mul_i32 s17, s16, s12
	s_sub_i32 s8, s8, s17
	s_add_i32 s22, s16, 1
	s_sub_i32 s17, s8, s12
	s_cmp_ge_u32 s8, s12
	s_cselect_b32 s16, s22, s16
	s_cselect_b32 s8, s17, s8
	s_add_i32 s17, s16, 1
	s_cmp_ge_u32 s8, s12
	s_cselect_b32 s8, s17, s16
	s_xor_b32 s8, s8, s13
	s_sub_i32 s8, s8, s13
	s_mul_i32 s11, s8, s11
	s_sub_i32 s9, s9, s11
	s_add_i32 s10, s9, s10
.LBB0_136:
	s_ashr_i32 s11, s10, 31
	s_lshl_b64 s[12:13], s[10:11], 19
	s_add_u32 s12, s27, s12
	s_addc_u32 s13, s28, s13
	s_cmp_eq_u32 s57, 2
	s_cselect_b32 s58, 0x40000, 0
	s_add_u32 s12, s12, s58
	s_addc_u32 s13, s13, 0
	s_and_b64 s[16:17], s[0:1], exec
	s_cselect_b32 s11, s13, s21
	s_cselect_b32 s51, s12, s20
	s_ashr_i32 s9, s8, 31
	s_lshl_b64 s[16:17], s[8:9], 19
	s_add_u32 s16, s29, s16
	s_addc_u32 s17, s30, s17
	s_and_b64 s[22:23], s[0:1], exec
	s_cselect_b32 s9, s17, s19
	s_cselect_b32 s52, s16, s18
	s_add_u32 s53, s18, 0x100
	s_addc_u32 s54, s19, 0
	s_add_u32 s18, s20, 0x40080
	v_mov_b32_e32 v2, 0
	s_addc_u32 s19, s21, 0
	s_mov_b32 s55, -2
	v_mov_b32_e32 v3, v2
	v_mov_b32_e32 v4, v2
	v_mov_b32_e32 v5, v2
	v_mov_b32_e32 v6, v2
	v_mov_b32_e32 v7, v2
	v_mov_b32_e32 v8, v2
	v_mov_b32_e32 v9, v2
	v_mov_b32_e32 v10, v2
	v_mov_b32_e32 v11, v2
	v_mov_b32_e32 v12, v2
	v_mov_b32_e32 v13, v2
	v_mov_b32_e32 v14, v2
	v_mov_b32_e32 v15, v2
	v_mov_b32_e32 v16, v2
	v_mov_b32_e32 v17, v2
	s_waitcnt vmcnt(0)
	v_mov_b32_e32 v18, v2
	v_mov_b32_e32 v19, v2
	v_mov_b32_e32 v20, v2
	v_mov_b32_e32 v21, v2
	v_mov_b32_e32 v22, v2
	v_mov_b32_e32 v23, v2
	v_mov_b32_e32 v24, v2
	v_mov_b32_e32 v25, v2
	v_mov_b32_e32 v38, v2
	v_mov_b32_e32 v39, v2
	v_mov_b32_e32 v40, v2
	v_mov_b32_e32 v41, v2
	v_mov_b32_e32 v42, v2
	v_mov_b32_e32 v43, v2
	v_mov_b32_e32 v44, v2
	v_mov_b32_e32 v45, v2
	v_mov_b32_e32 v26, v2
	v_mov_b32_e32 v27, v2
	v_mov_b32_e32 v28, v2
	v_mov_b32_e32 v29, v2
	v_mov_b32_e32 v30, v2
	v_mov_b32_e32 v31, v2
	v_mov_b32_e32 v32, v2
	v_mov_b32_e32 v33, v2
	v_mov_b32_e32 v46, v2
	v_mov_b32_e32 v47, v2
	v_mov_b32_e32 v48, v2
	v_mov_b32_e32 v49, v2
	v_mov_b32_e32 v50, v2
	v_mov_b32_e32 v51, v2
	v_mov_b32_e32 v52, v2
	v_mov_b32_e32 v53, v2
	v_mov_b32_e32 v54, v2
	v_mov_b32_e32 v55, v2
	v_mov_b32_e32 v56, v2
	v_mov_b32_e32 v57, v2
	v_mov_b32_e32 v58, v2
	v_mov_b32_e32 v59, v2
	v_mov_b32_e32 v60, v2
	v_mov_b32_e32 v61, v2
	v_mov_b32_e32 v62, v2
	v_mov_b32_e32 v63, v2
	v_mov_b32_e32 v64, v2
	v_mov_b32_e32 v65, v2
	v_mov_b32_e32 v66, v2
	v_mov_b32_e32 v67, v2
	v_mov_b32_e32 v68, v2
	v_mov_b32_e32 v69, v2
	v_mov_b32_e32 v70, v2
	v_mov_b32_e32 v71, v2
	v_mov_b32_e32 v72, v2
	v_mov_b32_e32 v73, v2
	v_mov_b32_e32 v74, v2
	v_mov_b32_e32 v75, v2
	v_mov_b32_e32 v76, v2
	v_mov_b32_e32 v77, v2
	v_mov_b32_e32 v78, v2
	v_mov_b32_e32 v79, v2
	v_mov_b32_e32 v80, v2
	v_mov_b32_e32 v81, v2
	v_mov_b32_e32 v82, v2
	v_mov_b32_e32 v83, v2
	v_mov_b32_e32 v84, v2
	v_mov_b32_e32 v85, v2
	v_mov_b32_e32 v86, v2
	v_mov_b32_e32 v87, v2
	v_mov_b32_e32 v88, v2
	v_mov_b32_e32 v89, v2
	v_mov_b32_e32 v90, v2
	v_mov_b32_e32 v91, v2
	v_mov_b32_e32 v92, v2
	v_mov_b32_e32 v93, v2
	v_mov_b32_e32 v102, v2
	v_mov_b32_e32 v103, v2
	v_mov_b32_e32 v104, v2
	v_mov_b32_e32 v105, v2
	v_mov_b32_e32 v106, v2
	v_mov_b32_e32 v107, v2
	v_mov_b32_e32 v108, v2
	v_mov_b32_e32 v109, v2
	v_mov_b32_e32 v94, v2
	v_mov_b32_e32 v95, v2
	v_mov_b32_e32 v96, v2
	v_mov_b32_e32 v97, v2
	v_mov_b32_e32 v98, v2
	v_mov_b32_e32 v99, v2
	v_mov_b32_e32 v100, v2
	v_mov_b32_e32 v101, v2
	v_mov_b32_e32 v110, v2
	v_mov_b32_e32 v111, v2
	v_mov_b32_e32 v112, v2
	v_mov_b32_e32 v113, v2
	v_mov_b32_e32 v114, v2
	v_mov_b32_e32 v115, v2
	v_mov_b32_e32 v116, v2
	v_mov_b32_e32 v117, v2
	v_mov_b32_e32 v118, v2
	v_mov_b32_e32 v119, v2
	v_mov_b32_e32 v120, v2
	v_mov_b32_e32 v121, v2
	v_mov_b32_e32 v122, v2
	v_mov_b32_e32 v123, v2
	v_mov_b32_e32 v124, v2
	v_mov_b32_e32 v125, v2
	v_mov_b32_e32 v126, v2
	v_mov_b32_e32 v127, v2
	v_mov_b32_e32 v128, v2
	v_mov_b32_e32 v129, v2
	v_mov_b32_e32 v130, v2
	v_mov_b32_e32 v131, v2
	v_mov_b32_e32 v132, v2
	v_mov_b32_e32 v133, v2
.LBB0_137:
	s_add_u32 s20, s18, 0xfffc0080
	s_addc_u32 s21, s19, -1
	s_add_i32 s33, 0, 0x10000
	s_cmp_eq_u32 s55, 12
	s_cselect_b32 s23, s11, s21
	s_cselect_b32 s22, s51, s20
	s_cselect_b32 s21, s9, s54
	s_cselect_b32 s20, s52, s53
	s_add_i32 s44, 0, 0x14000
	v_add_u32_e32 v158, s33, v163
	v_add_u32_e32 v178, s44, v163
	ds_read_b128 v[146:149], v158
	ds_read_b128 v[150:153], v158 offset:1024
	ds_read_b128 v[154:157], v158 offset:2048
	ds_read_b128 v[158:161], v158 offset:3072
	ds_read_b128 v[166:169], v178
	ds_read_b128 v[170:173], v178 offset:1024
	ds_read_b128 v[174:177], v178 offset:2048
	ds_read_b128 v[178:181], v178 offset:3072
	v_lshl_add_u64 v[182:183], s[18:19], 0, v[144:145]
	s_add_i32 m0, s15, 0xc000
	ds_read_b128 v[186:189], v165
	ds_read_b128 v[190:193], v165 offset:1024
	ds_read_b128 v[194:197], v165 offset:2048
	ds_read_b128 v[198:201], v165 offset:3072
	ds_read_b128 v[224:227], v165 offset:4096
	ds_read_b128 v[228:231], v165 offset:5120
	ds_read_b128 v[232:235], v165 offset:6144
	ds_read_b128 v[236:239], v165 offset:7168
	s_cmp_lg_u32 s56, 0
	s_cbranch_scc1 .Lhf_d1
	global_load_lds_dwordx4 v[182:183], off
.Lhf_d1:
	v_lshl_add_u64 v[182:183], s[18:19], 0, v[142:143]
	s_add_i32 m0, s15, 0xe000
	s_nop 0
	s_cmp_lg_u32 s56, 0
	s_cbranch_scc1 .Lhf_d2
	global_load_lds_dwordx4 v[182:183], off
.Lhf_d2:
	s_cmp_lg_u32 s56, 0
	s_cbranch_scc1 .Lhf_w1
	s_waitcnt vmcnt(8)
	s_branch .Lhf_we1
.Lhf_w1:
	s_waitcnt vmcnt(6)
.Lhf_we1:
	s_waitcnt lgkmcnt(0)
	s_barrier
	s_setprio 1
	s_waitcnt lgkmcnt(0)
	v_mfma_f32_16x16x32_bf16 v[130:133], v[146:149], v[186:189], v[130:133]
	v_mfma_f32_16x16x32_bf16 v[126:129], v[154:157], v[186:189], v[126:129]
	v_mfma_f32_16x16x32_bf16 v[122:125], v[146:149], v[194:197], v[122:125]
	v_mfma_f32_16x16x32_bf16 v[118:121], v[154:157], v[194:197], v[118:121]
	v_mfma_f32_16x16x32_bf16 v[114:117], v[146:149], v[224:227], v[114:117]
	v_mfma_f32_16x16x32_bf16 v[110:113], v[154:157], v[224:227], v[110:113]
	v_mfma_f32_16x16x32_bf16 v[98:101], v[146:149], v[232:235], v[98:101]
	v_mfma_f32_16x16x32_bf16 v[94:97], v[154:157], v[232:235], v[94:97]
	v_mfma_f32_16x16x32_bf16 v[130:133], v[150:153], v[190:193], v[130:133]
	v_mfma_f32_16x16x32_bf16 v[126:129], v[158:161], v[190:193], v[126:129]
	v_mfma_f32_16x16x32_bf16 v[122:125], v[150:153], v[198:201], v[122:125]
	v_mfma_f32_16x16x32_bf16 v[118:121], v[158:161], v[198:201], v[118:121]
	v_mfma_f32_16x16x32_bf16 v[114:117], v[150:153], v[228:231], v[114:117]
	v_mfma_f32_16x16x32_bf16 v[110:113], v[158:161], v[228:231], v[110:113]
	v_mfma_f32_16x16x32_bf16 v[98:101], v[150:153], v[236:239], v[98:101]
	v_mfma_f32_16x16x32_bf16 v[94:97], v[158:161], v[236:239], v[94:97]
	s_setprio 0
	s_setprio 1
	v_mfma_f32_16x16x32_bf16 v[106:109], v[166:169], v[186:189], v[106:109]
	v_mfma_f32_16x16x32_bf16 v[102:105], v[174:177], v[186:189], v[102:105]
	v_mfma_f32_16x16x32_bf16 v[90:93], v[166:169], v[194:197], v[90:93]
	v_mfma_f32_16x16x32_bf16 v[86:89], v[174:177], v[194:197], v[86:89]
	v_mfma_f32_16x16x32_bf16 v[82:85], v[166:169], v[224:227], v[82:85]
	v_mfma_f32_16x16x32_bf16 v[78:81], v[174:177], v[224:227], v[78:81]
	v_mfma_f32_16x16x32_bf16 v[74:77], v[166:169], v[232:235], v[74:77]
	v_mfma_f32_16x16x32_bf16 v[70:73], v[174:177], v[232:235], v[70:73]
	v_mfma_f32_16x16x32_bf16 v[106:109], v[170:173], v[190:193], v[106:109]
	v_mfma_f32_16x16x32_bf16 v[102:105], v[178:181], v[190:193], v[102:105]
	v_mfma_f32_16x16x32_bf16 v[90:93], v[170:173], v[198:201], v[90:93]
	v_mfma_f32_16x16x32_bf16 v[86:89], v[178:181], v[198:201], v[86:89]
	v_mfma_f32_16x16x32_bf16 v[82:85], v[170:173], v[228:231], v[82:85]
	v_mfma_f32_16x16x32_bf16 v[78:81], v[178:181], v[228:231], v[78:81]
	v_mfma_f32_16x16x32_bf16 v[74:77], v[170:173], v[236:239], v[74:77]
	v_mfma_f32_16x16x32_bf16 v[70:73], v[178:181], v[236:239], v[70:73]
	s_setprio 0
	s_barrier
	s_add_i32 s33, s33, s31
	v_lshl_add_u64 v[182:183], s[20:21], 0, v[0:1]
	s_mov_b32 m0, s33
	s_cmp_lg_u32 s56, 0
	s_cbranch_scc1 .Lhf_r2
	ds_read_b128 v[186:189], v165 offset:16384
	ds_read_b128 v[190:193], v165 offset:17408
	ds_read_b128 v[194:197], v165 offset:18432
	ds_read_b128 v[198:201], v165 offset:19456
	ds_read_b128 v[224:227], v165 offset:20480
	ds_read_b128 v[228:231], v165 offset:21504
	ds_read_b128 v[232:235], v165 offset:22528
	ds_read_b128 v[236:239], v165 offset:23552
.Lhf_r2:
	global_load_lds_dwordx4 v[182:183], off
	s_add_i32 m0, s33, 0x2000
	s_add_u32 s40, s20, 0x40000
	v_lshl_add_u64 v[184:185], s[20:21], 0, v[134:135]
	s_addc_u32 s41, s21, 0
	s_add_i32 s33, s44, s31
	global_load_lds_dwordx4 v[184:185], off
	v_lshl_add_u64 v[202:203], s[40:41], 0, v[0:1]
	s_mov_b32 m0, s33
	v_lshl_add_u64 v[210:211], s[22:23], 0, v[136:137]
	global_load_lds_dwordx4 v[202:203], off
	v_lshl_add_u64 v[202:203], s[40:41], 0, v[134:135]
	s_add_i32 m0, s33, 0x2000
	s_nop 0
	global_load_lds_dwordx4 v[202:203], off
	v_lshl_add_u64 v[202:203], s[22:23], 0, v[138:139]
	s_mov_b32 m0, s15
	s_nop 0
	global_load_lds_dwordx4 v[202:203], off
	s_mov_b32 m0, s35
	s_nop 0
	global_load_lds_dwordx4 v[210:211], off
	s_cmp_lg_u32 s56, 0
	s_cbranch_scc1 .Lhf_w2
	s_waitcnt vmcnt(8)
	s_branch .Lhf_we2

.Lhf_we2:
	s_waitcnt lgkmcnt(0)
	s_barrier
	s_cmp_lg_u32 s56, 0
	s_cbranch_scc1 .Lhf_m2
	s_setprio 1
	s_waitcnt lgkmcnt(0)
	v_mfma_f32_16x16x32_bf16 v[66:69], v[146:149], v[186:189], v[66:69]
	v_mfma_f32_16x16x32_bf16 v[62:65], v[154:157], v[186:189], v[62:65]
	v_mfma_f32_16x16x32_bf16 v[58:61], v[146:149], v[194:197], v[58:61]
	v_mfma_f32_16x16x32_bf16 v[54:57], v[154:157], v[194:197], v[54:57]
	v_mfma_f32_16x16x32_bf16 v[50:53], v[146:149], v[224:227], v[50:53]
	v_mfma_f32_16x16x32_bf16 v[46:49], v[154:157], v[224:227], v[46:49]
	v_mfma_f32_16x16x32_bf16 v[30:33], v[146:149], v[232:235], v[30:33]
	v_mfma_f32_16x16x32_bf16 v[26:29], v[154:157], v[232:235], v[26:29]
	v_mfma_f32_16x16x32_bf16 v[66:69], v[150:153], v[190:193], v[66:69]
	v_mfma_f32_16x16x32_bf16 v[62:65], v[158:161], v[190:193], v[62:65]
	v_mfma_f32_16x16x32_bf16 v[58:61], v[150:153], v[198:201], v[58:61]
	v_mfma_f32_16x16x32_bf16 v[54:57], v[158:161], v[198:201], v[54:57]
	v_mfma_f32_16x16x32_bf16 v[50:53], v[150:153], v[228:231], v[50:53]
	v_mfma_f32_16x16x32_bf16 v[46:49], v[158:161], v[228:231], v[46:49]
	v_mfma_f32_16x16x32_bf16 v[30:33], v[150:153], v[236:239], v[30:33]
	v_mfma_f32_16x16x32_bf16 v[26:29], v[158:161], v[236:239], v[26:29]
	s_setprio 0
	s_setprio 1
	v_mfma_f32_16x16x32_bf16 v[42:45], v[166:169], v[186:189], v[42:45]
	v_mfma_f32_16x16x32_bf16 v[38:41], v[174:177], v[186:189], v[38:41]
	v_mfma_f32_16x16x32_bf16 v[22:25], v[166:169], v[194:197], v[22:25]
	v_mfma_f32_16x16x32_bf16 v[18:21], v[174:177], v[194:197], v[18:21]
	v_mfma_f32_16x16x32_bf16 v[14:17], v[166:169], v[224:227], v[14:17]
	v_mfma_f32_16x16x32_bf16 v[10:13], v[174:177], v[224:227], v[10:13]
	v_mfma_f32_16x16x32_bf16 v[6:9], v[166:169], v[232:235], v[6:9]
	v_mfma_f32_16x16x32_bf16 v[2:5], v[174:177], v[232:235], v[2:5]
	v_mfma_f32_16x16x32_bf16 v[42:45], v[170:173], v[190:193], v[42:45]
	v_mfma_f32_16x16x32_bf16 v[38:41], v[178:181], v[190:193], v[38:41]
	v_mfma_f32_16x16x32_bf16 v[22:25], v[170:173], v[198:201], v[22:25]
	v_mfma_f32_16x16x32_bf16 v[18:21], v[178:181], v[198:201], v[18:21]
	v_mfma_f32_16x16x32_bf16 v[14:17], v[170:173], v[228:231], v[14:17]
	v_mfma_f32_16x16x32_bf16 v[10:13], v[178:181], v[228:231], v[10:13]
	v_mfma_f32_16x16x32_bf16 v[6:9], v[170:173], v[236:239], v[6:9]
	v_mfma_f32_16x16x32_bf16 v[2:5], v[178:181], v[236:239], v[2:5]
	s_setprio 0
.Lhf_m2:
	s_barrier
	s_add_i32 s33, 0, 0x18000
	s_add_i32 s40, 0, 0x1c000
	v_add_u32_e32 v158, s33, v163
	v_add_u32_e32 v178, s40, v163
	ds_read_b128 v[146:149], v158
	ds_read_b128 v[150:153], v158 offset:1024
	ds_read_b128 v[154:157], v158 offset:2048
	ds_read_b128 v[158:161], v158 offset:3072
	ds_read_b128 v[166:169], v178
	ds_read_b128 v[170:173], v178 offset:1024
	ds_read_b128 v[174:177], v178 offset:2048
	ds_read_b128 v[178:181], v178 offset:3072
	s_add_u32 s22, s22, 0x40000
	s_addc_u32 s23, s23, 0
	s_mov_b32 m0, s36
	v_lshl_add_u64 v[218:219], s[22:23], 0, v[138:139]
	ds_read_b128 v[186:189], v165 offset:32768
	ds_read_b128 v[190:193], v165 offset:33792
	ds_read_b128 v[194:197], v165 offset:34816
	ds_read_b128 v[198:201], v165 offset:35840
	ds_read_b128 v[224:227], v165 offset:36864
	ds_read_b128 v[228:231], v165 offset:37888
	ds_read_b128 v[232:235], v165 offset:38912
	ds_read_b128 v[236:239], v165 offset:39936
	s_cmp_lg_u32 s56, 0
	s_cbranch_scc1 .Lhf_d3
	global_load_lds_dwordx4 v[218:219], off
.Lhf_d3:
	v_lshl_add_u64 v[218:219], s[22:23], 0, v[136:137]
	s_mov_b32 m0, s37
	s_nop 0
	s_cmp_lg_u32 s56, 0
	s_cbranch_scc1 .Lhf_d4
	global_load_lds_dwordx4 v[218:219], off

.Lhf_we3:
	s_waitcnt lgkmcnt(0)
	s_barrier
	s_setprio 1
	s_waitcnt lgkmcnt(0)
	v_mfma_f32_16x16x32_bf16 v[130:133], v[146:149], v[186:189], v[130:133]
	v_mfma_f32_16x16x32_bf16 v[126:129], v[154:157], v[186:189], v[126:129]
	v_mfma_f32_16x16x32_bf16 v[122:125], v[146:149], v[194:197], v[122:125]
	v_mfma_f32_16x16x32_bf16 v[118:121], v[154:157], v[194:197], v[118:121]
	v_mfma_f32_16x16x32_bf16 v[114:117], v[146:149], v[224:227], v[114:117]
	v_mfma_f32_16x16x32_bf16 v[110:113], v[154:157], v[224:227], v[110:113]
	v_mfma_f32_16x16x32_bf16 v[98:101], v[146:149], v[232:235], v[98:101]
	v_mfma_f32_16x16x32_bf16 v[94:97], v[154:157], v[232:235], v[94:97]
	v_mfma_f32_16x16x32_bf16 v[130:133], v[150:153], v[190:193], v[130:133]
	v_mfma_f32_16x16x32_bf16 v[126:129], v[158:161], v[190:193], v[126:129]
	v_mfma_f32_16x16x32_bf16 v[122:125], v[150:153], v[198:201], v[122:125]
	v_mfma_f32_16x16x32_bf16 v[118:121], v[158:161], v[198:201], v[118:121]
	v_mfma_f32_16x16x32_bf16 v[114:117], v[150:153], v[228:231], v[114:117]
	v_mfma_f32_16x16x32_bf16 v[110:113], v[158:161], v[228:231], v[110:113]
	v_mfma_f32_16x16x32_bf16 v[98:101], v[150:153], v[236:239], v[98:101]
	v_mfma_f32_16x16x32_bf16 v[94:97], v[158:161], v[236:239], v[94:97]
	s_setprio 0
	s_setprio 1
	v_mfma_f32_16x16x32_bf16 v[106:109], v[166:169], v[186:189], v[106:109]
	v_mfma_f32_16x16x32_bf16 v[102:105], v[174:177], v[186:189], v[102:105]
	v_mfma_f32_16x16x32_bf16 v[90:93], v[166:169], v[194:197], v[90:93]
	v_mfma_f32_16x16x32_bf16 v[86:89], v[174:177], v[194:197], v[86:89]
	v_mfma_f32_16x16x32_bf16 v[82:85], v[166:169], v[224:227], v[82:85]
	v_mfma_f32_16x16x32_bf16 v[78:81], v[174:177], v[224:227], v[78:81]
	v_mfma_f32_16x16x32_bf16 v[74:77], v[166:169], v[232:235], v[74:77]
	v_mfma_f32_16x16x32_bf16 v[70:73], v[174:177], v[232:235], v[70:73]
	v_mfma_f32_16x16x32_bf16 v[106:109], v[170:173], v[190:193], v[106:109]
	v_mfma_f32_16x16x32_bf16 v[102:105], v[178:181], v[190:193], v[102:105]
	v_mfma_f32_16x16x32_bf16 v[90:93], v[170:173], v[198:201], v[90:93]
	v_mfma_f32_16x16x32_bf16 v[86:89], v[178:181], v[198:201], v[86:89]
	v_mfma_f32_16x16x32_bf16 v[82:85], v[170:173], v[228:231], v[82:85]
	v_mfma_f32_16x16x32_bf16 v[78:81], v[178:181], v[228:231], v[78:81]
	v_mfma_f32_16x16x32_bf16 v[74:77], v[170:173], v[236:239], v[74:77]
	v_mfma_f32_16x16x32_bf16 v[70:73], v[178:181], v[236:239], v[70:73]
	s_setprio 0
	s_barrier
	s_add_i32 s22, s33, s31
	v_lshl_add_u64 v[182:183], v[182:183], 0, s[46:47]
	s_mov_b32 m0, s22
	s_cmp_lg_u32 s56, 0
	s_cbranch_scc1 .Lhf_r4
	ds_read_b128 v[186:189], v165 offset:49152
	ds_read_b128 v[190:193], v165 offset:50176
	ds_read_b128 v[194:197], v165 offset:51200
	ds_read_b128 v[198:201], v165 offset:52224
	ds_read_b128 v[224:227], v165 offset:53248
	ds_read_b128 v[228:231], v165 offset:54272
	ds_read_b128 v[232:235], v165 offset:55296
	ds_read_b128 v[236:239], v165 offset:56320
.Lhf_r4:
	global_load_lds_dwordx4 v[182:183], off
	s_add_i32 m0, s22, 0x2000
	s_add_u32 s20, s20, 0x40080
	v_lshl_add_u64 v[182:183], v[184:185], 0, s[46:47]
	s_addc_u32 s21, s21, 0
	s_add_i32 s22, s40, s31
	global_load_lds_dwordx4 v[182:183], off
	v_lshl_add_u64 v[182:183], s[20:21], 0, v[0:1]
	s_mov_b32 m0, s22
	s_nop 0
	global_load_lds_dwordx4 v[182:183], off
	v_lshl_add_u64 v[182:183], s[20:21], 0, v[134:135]
	s_add_i32 m0, s22, 0x2000
	s_nop 0
	global_load_lds_dwordx4 v[182:183], off
	v_lshl_add_u64 v[182:183], v[202:203], 0, s[46:47]
	s_mov_b32 m0, s38
	s_nop 0
	global_load_lds_dwordx4 v[182:183], off
	v_lshl_add_u64 v[182:183], v[210:211], 0, s[46:47]
	s_mov_b32 m0, s39
	s_nop 0
	global_load_lds_dwordx4 v[182:183], off
	s_cmp_lg_u32 s56, 0
	s_cbranch_scc1 .Lhf_w4
	s_waitcnt vmcnt(8)
	s_branch .Lhf_we4

.Lhf_m4:
	s_barrier
	s_add_i32 s55, s55, 2
	s_add_u32 s53, s53, 0x100
	s_addc_u32 s54, s54, 0
	s_add_u32 s18, s18, 0x100
	s_addc_u32 s19, s19, 0
	s_cmp_gt_u32 s55, 13
	s_cbranch_scc0 .LBB0_137
	s_and_b64 vcc, exec, s[6:7]
	s_cbranch_vccz .LBB0_140
	s_barrier
.LBB0_140:
	v_lshl_or_b32 v148, s50, 8, v164
	v_lshl_add_u32 v146, s14, 8, v162
	s_cmp_eq_u32 s56, 2
	s_cselect_b32 s58, 0x80, 0
	v_add_u32_e32 v146, s58, v146
	v_ashrrev_i32_e32 v149, 31, v148
	v_mov_b64_e32 v[170:171], s[4:5]
	s_movk_i32 s9, 0x1c00
	v_mad_i64_i32 v[150:151], s[18:19], v146, s9, v[170:171]
	v_lshlrev_b64 v[172:173], 1, v[148:149]
	v_lshl_add_u64 v[152:153], v[150:151], 0, v[172:173]
	v_cvt_pk_bf16_f32 v148, v130, v131
	v_cvt_pk_bf16_f32 v149, v132, v133
	v_cvt_pk_bf16_f32 v150, v126, v127
	v_cvt_pk_bf16_f32 v151, v128, v129
	global_store_dwordx4 v[152:153], v[148:151], off
	v_cvt_pk_bf16_f32 v168, v46, v47
	v_cvt_pk_bf16_f32 v169, v48, v49
	v_cvt_pk_bf16_f32 v148, v106, v107
	v_cvt_pk_bf16_f32 v149, v108, v109
	v_cvt_pk_bf16_f32 v150, v102, v103
	v_cvt_pk_bf16_f32 v151, v104, v105
	global_store_dwordx4 v[152:153], v[148:151], off offset:256
	v_cvt_pk_bf16_f32 v152, v118, v119
	v_cvt_pk_bf16_f32 v153, v120, v121
	v_or_b32_e32 v148, 16, v146
	v_mad_i64_i32 v[150:151], s[18:19], v148, s9, v[170:171]
	v_lshl_add_u64 v[154:155], v[150:151], 0, v[172:173]
	v_cvt_pk_bf16_f32 v150, v122, v123
	v_cvt_pk_bf16_f32 v151, v124, v125
	global_store_dwordx4 v[154:155], v[150:153], off
	s_cmp_lg_u32 s50, 13
	s_nop 0
	v_cvt_pk_bf16_f32 v150, v90, v91
	v_cvt_pk_bf16_f32 v151, v92, v93
	v_cvt_pk_bf16_f32 v152, v86, v87
	v_cvt_pk_bf16_f32 v153, v88, v89
	global_store_dwordx4 v[154:155], v[150:153], off offset:256
	v_cvt_pk_bf16_f32 v154, v110, v111
	v_cvt_pk_bf16_f32 v155, v112, v113
	v_or_b32_e32 v150, 32, v146
	v_mad_i64_i32 v[152:153], s[18:19], v150, s9, v[170:171]
	v_lshl_add_u64 v[156:157], v[152:153], 0, v[172:173]
	v_cvt_pk_bf16_f32 v152, v114, v115
	v_cvt_pk_bf16_f32 v153, v116, v117
	global_store_dwordx4 v[156:157], v[152:155], off
	s_nop 1
	v_cvt_pk_bf16_f32 v152, v82, v83
	v_cvt_pk_bf16_f32 v153, v84, v85
	v_cvt_pk_bf16_f32 v154, v78, v79
	v_cvt_pk_bf16_f32 v155, v80, v81
	global_store_dwordx4 v[156:157], v[152:155], off offset:256
	v_cvt_pk_bf16_f32 v156, v94, v95
	v_cvt_pk_bf16_f32 v157, v96, v97
	v_or_b32_e32 v152, 48, v146
	v_mad_i64_i32 v[154:155], s[18:19], v152, s9, v[170:171]
	v_lshl_add_u64 v[158:159], v[154:155], 0, v[172:173]
	v_cvt_pk_bf16_f32 v154, v98, v99
	v_cvt_pk_bf16_f32 v155, v100, v101
	global_store_dwordx4 v[158:159], v[154:157], off
	s_nop 1
	v_cvt_pk_bf16_f32 v154, v74, v75
	v_cvt_pk_bf16_f32 v155, v76, v77
	v_cvt_pk_bf16_f32 v156, v70, v71
	v_cvt_pk_bf16_f32 v157, v72, v73
	global_store_dwordx4 v[158:159], v[154:157], off offset:256
	s_cmp_lg_u32 s56, 0
	s_cbranch_scc1 .Lhf_e1
	v_cvt_pk_bf16_f32 v158, v62, v63
	v_cvt_pk_bf16_f32 v159, v64, v65
	v_add_u32_e32 v154, 0x80, v146
	v_mad_i64_i32 v[156:157], s[18:19], v154, s9, v[170:171]
	v_lshl_add_u64 v[160:161], v[156:157], 0, v[172:173]
	v_cvt_pk_bf16_f32 v156, v66, v67
	v_cvt_pk_bf16_f32 v157, v68, v69
	global_store_dwordx4 v[160:161], v[156:159], off
	s_nop 1
	v_cvt_pk_bf16_f32 v156, v42, v43
	v_cvt_pk_bf16_f32 v157, v44, v45
	v_cvt_pk_bf16_f32 v158, v38, v39
	v_cvt_pk_bf16_f32 v159, v40, v41
	global_store_dwordx4 v[160:161], v[156:159], off offset:256
	v_cvt_pk_bf16_f32 v160, v54, v55
	v_cvt_pk_bf16_f32 v161, v56, v57
	v_add_u32_e32 v156, 0x90, v146
	v_mad_i64_i32 v[158:159], s[18:19], v156, s9, v[170:171]
	v_lshl_add_u64 v[166:167], v[158:159], 0, v[172:173]
	v_cvt_pk_bf16_f32 v158, v58, v59
	v_cvt_pk_bf16_f32 v159, v60, v61
	global_store_dwordx4 v[166:167], v[158:161], off
	s_nop 1
	v_cvt_pk_bf16_f32 v158, v22, v23
	v_cvt_pk_bf16_f32 v159, v24, v25
	v_cvt_pk_bf16_f32 v160, v18, v19
	v_cvt_pk_bf16_f32 v161, v20, v21
	global_store_dwordx4 v[166:167], v[158:161], off offset:256
	v_cvt_pk_bf16_f32 v166, v50, v51
	v_cvt_pk_bf16_f32 v167, v52, v53
	v_add_u32_e32 v158, 0xa0, v146
	v_mad_i64_i32 v[160:161], s[18:19], v158, s9, v[170:171]
	v_lshl_add_u64 v[160:161], v[160:161], 0, v[172:173]
	global_store_dwordx4 v[160:161], v[166:169], off
	s_nop 1
	v_cvt_pk_bf16_f32 v166, v14, v15
	v_cvt_pk_bf16_f32 v167, v16, v17
	v_cvt_pk_bf16_f32 v168, v10, v11
	v_cvt_pk_bf16_f32 v169, v12, v13
	global_store_dwordx4 v[160:161], v[166:169], off offset:256
	v_add_u32_e32 v160, 0xb0, v146
	s_nop 0
	v_mad_i64_i32 v[166:167], s[18:19], v160, s9, v[170:171]
	v_lshl_add_u64 v[170:171], v[166:167], 0, v[172:173]
	v_cvt_pk_bf16_f32 v166, v30, v31
	v_cvt_pk_bf16_f32 v167, v32, v33
	v_cvt_pk_bf16_f32 v168, v26, v27
	v_cvt_pk_bf16_f32 v169, v28, v29
	global_store_dwordx4 v[170:171], v[166:169], off
	s_nop 1
	v_cvt_pk_bf16_f32 v166, v6, v7
	v_cvt_pk_bf16_f32 v167, v8, v9
	v_cvt_pk_bf16_f32 v168, v2, v3
	v_cvt_pk_bf16_f32 v169, v4, v5
	global_store_dwordx4 v[170:171], v[166:169], off offset:256
.Lhf_e1:
	s_cmp_lg_u32 s50, 13
	s_cbranch_scc1 .LBB0_142
	v_ashrrev_i32_e32 v147, 31, v146
	v_lshlrev_b64 v[146:147], 10, v[146:147]
	v_ashrrev_i32_e32 v149, 31, v148
	v_lshl_add_u64 v[146:147], v[140:141], 0, v[146:147]
	global_store_dwordx4 v[146:147], v[130:133], off
	global_store_dwordx4 v[146:147], v[126:129], off offset:16
	global_store_dwordx4 v[146:147], v[106:109], off offset:512
	global_store_dwordx4 v[146:147], v[102:105], off offset:528
	v_ashrrev_i32_e32 v151, 31, v150
	v_ashrrev_i32_e32 v153, 31, v152
	v_lshlrev_b64 v[102:103], 10, v[148:149]
	v_lshl_add_u64 v[102:103], v[140:141], 0, v[102:103]
	global_store_dwordx4 v[102:103], v[122:125], off
	global_store_dwordx4 v[102:103], v[118:121], off offset:16
	global_store_dwordx4 v[102:103], v[90:93], off offset:512
	global_store_dwordx4 v[102:103], v[86:89], off offset:528
	v_ashrrev_i32_e32 v155, 31, v154
	v_ashrrev_i32_e32 v157, 31, v156
	v_lshlrev_b64 v[86:87], 10, v[150:151]
	v_lshl_add_u64 v[86:87], v[140:141], 0, v[86:87]
	global_store_dwordx4 v[86:87], v[114:117], off
	global_store_dwordx4 v[86:87], v[110:113], off offset:16
	global_store_dwordx4 v[86:87], v[82:85], off offset:512
	global_store_dwordx4 v[86:87], v[78:81], off offset:528
	v_ashrrev_i32_e32 v159, 31, v158
	v_ashrrev_i32_e32 v161, 31, v160
	v_lshlrev_b64 v[78:79], 10, v[152:153]
	v_lshl_add_u64 v[78:79], v[140:141], 0, v[78:79]
	global_store_dwordx4 v[78:79], v[98:101], off
	global_store_dwordx4 v[78:79], v[94:97], off offset:16
	global_store_dwordx4 v[78:79], v[74:77], off offset:512
	global_store_dwordx4 v[78:79], v[70:73], off offset:528
	s_cmp_lg_u32 s56, 0
	s_cbranch_scc1 .LBB0_142
	s_nop 1
	v_lshlrev_b64 v[70:71], 10, v[154:155]
	v_lshl_add_u64 v[70:71], v[140:141], 0, v[70:71]
	global_store_dwordx4 v[70:71], v[66:69], off
	global_store_dwordx4 v[70:71], v[62:65], off offset:16
	global_store_dwordx4 v[70:71], v[42:45], off offset:512
	global_store_dwordx4 v[70:71], v[38:41], off offset:528
	s_nop 1
	v_lshlrev_b64 v[38:39], 10, v[156:157]
	v_lshl_add_u64 v[38:39], v[140:141], 0, v[38:39]
	global_store_dwordx4 v[38:39], v[58:61], off
	global_store_dwordx4 v[38:39], v[54:57], off offset:16
	global_store_dwordx4 v[38:39], v[22:25], off offset:512
	global_store_dwordx4 v[38:39], v[18:21], off offset:528
	s_nop 1
	v_lshlrev_b64 v[18:19], 10, v[158:159]
	v_lshl_add_u64 v[18:19], v[140:141], 0, v[18:19]
	global_store_dwordx4 v[18:19], v[50:53], off
	global_store_dwordx4 v[18:19], v[46:49], off offset:16
	global_store_dwordx4 v[18:19], v[14:17], off offset:512
	global_store_dwordx4 v[18:19], v[10:13], off offset:528
	s_nop 1
	v_lshlrev_b64 v[10:11], 10, v[160:161]
	v_lshl_add_u64 v[10:11], v[140:141], 0, v[10:11]
	global_store_dwordx4 v[10:11], v[30:33], off
	global_store_dwordx4 v[10:11], v[26:29], off offset:16
	global_store_dwordx4 v[10:11], v[6:9], off offset:512
	global_store_dwordx4 v[10:11], v[2:5], off offset:528
